# grid barrier: non-leader workgroups poll the cross-XCD release generation directly instead of waiting for the per-XCC re-release (on top of the early L1 invalidate)
# speedup vs baseline: 1.0159x; 1.0024x over previous
; __device__ __forceinline__ unsigned xb_ld(unsigned* p)              { return __hip_atomic_load(p, __ATOMIC_RELAXED, __HIP_MEMORY_SCOPE_AGENT); }
; __device__ __forceinline__ unsigned xb_add(unsigned* p, unsigned v) { return __hip_atomic_fetch_add(p, v, __ATOMIC_RELAXED, __HIP_MEMORY_SCOPE_AGENT); }
; #define XB_SPIN(cond, bar) do { unsigned _sp = 0; while (cond) { __builtin_amdgcn_s_sleep(1); \
;     if ((++_sp & 255u) == 0u) { if (xb_ld(&(bar)[XB_TMO])) break; if (_sp > XB_SPIN_CAP) { atomicAdd(&(bar)[XB_TMO], 1u); break; } } } } while (0)
; __device__ __forceinline__ void xcd_barrier(const XcdBarrier& b, const bool xb_leader) {
;     ...
;         const unsigned old = xb_add(&bar[XB_XSUB(b.x)], 1u);
;         const unsigned gen = old / nloc;
;         if (old + 1u == (gen + 1u) * nloc) {
;             __builtin_amdgcn_fence(__ATOMIC_RELEASE, "agent");
;             asm volatile("s_waitcnt vmcnt(0)" ::: "memory");
;             const unsigned og = xb_add(&bar[XB_TOP], 1u);
;             const unsigned tg = og / nx;
;             if (og + 1u == (tg + 1u) * nx) xb_add(&bar[XB_TOPGEN], 1u);
;             else XB_SPIN(xb_ld(&bar[XB_TOPGEN]) == tg, bar);
;             __builtin_amdgcn_fence(__ATOMIC_ACQUIRE, "agent");
;             xb_add(&bar[XB_XGEN(b.x)], 1u);
;             asm volatile("s_waitcnt vmcnt(0)" ::: "memory");
;         } else {
;             XB_SPIN(xb_ld(&bar[XB_XGEN(b.x)]) == gen, bar);
;             __builtin_amdgcn_fence(__ATOMIC_ACQUIRE, "agent");
.LBB0_87:
	s_or_b64 exec, exec, s[12:13]
	v_cvt_f32_u32_e32 v2, v9
	s_waitcnt vmcnt(0)
	v_readfirstlane_b32 s3, v1
	v_sub_u32_e32 v1, 0, v9
	v_rcp_iflag_f32_e32 v2, v2
	v_add_u32_e32 v3, s3, v0
	v_mul_f32_e32 v2, 0x4f7ffffe, v2
	v_cvt_u32_f32_e32 v2, v2
	v_mul_lo_u32 v0, v1, v2
	v_mul_hi_u32 v0, v2, v0
	v_add_u32_e32 v0, v2, v0
	v_mul_hi_u32 v0, v3, v0
	v_mul_lo_u32 v1, v0, v9
	v_sub_u32_e32 v1, v3, v1
	v_add_u32_e32 v2, 1, v0
	v_cmp_ge_u32_e32 vcc, v1, v9
	s_nop 1
	v_cndmask_b32_e32 v0, v0, v2, vcc
	v_sub_u32_e32 v2, v1, v9
	v_cndmask_b32_e32 v1, v1, v2, vcc
	v_add_u32_e32 v2, 1, v0
	v_cmp_ge_u32_e32 vcc, v1, v9
	v_add_u32_e32 v1, 1, v3
	s_nop 0
	v_cndmask_b32_e32 v0, v0, v2, vcc
	v_mul_lo_u32 v2, v9, v0
	v_add_u32_e32 v2, v2, v9
	v_cmp_ne_u32_e32 vcc, v1, v2
	s_and_saveexec_b64 s[6:7], vcc
	s_xor_b64 s[6:7], exec, s[6:7]
	s_cbranch_execz .LBB0_101
	v_mov_b32_e32 v1, 0x3100
	global_load_dword v1, v1, s[28:29] offset:1024 sc1
	s_add_u32 s14, s28, 0x3500
	s_addc_u32 s15, s29, 0
	s_waitcnt vmcnt(0)
	v_cmp_eq_u32_e32 vcc, v1, v0
	s_and_saveexec_b64 s[12:13], vcc
	s_cbranch_execz .LBB0_100
	s_mov_b32 s3, 1
	s_mov_b64 s[16:17], 0
	v_mov_b32_e32 v1, 0
	s_branch .LBB0_91

; __device__ __forceinline__ unsigned xb_ld(unsigned* p)              { return __hip_atomic_load(p, __ATOMIC_RELAXED, __HIP_MEMORY_SCOPE_AGENT); }
; __device__ __forceinline__ unsigned xb_add(unsigned* p, unsigned v) { return __hip_atomic_fetch_add(p, v, __ATOMIC_RELAXED, __HIP_MEMORY_SCOPE_AGENT); }
; #define XB_SPIN(cond, bar) do { unsigned _sp = 0; while (cond) { __builtin_amdgcn_s_sleep(1); \
;     if ((++_sp & 255u) == 0u) { if (xb_ld(&(bar)[XB_TMO])) break; if (_sp > XB_SPIN_CAP) { atomicAdd(&(bar)[XB_TMO], 1u); break; } } } } while (0)
; __device__ __forceinline__ void xcd_barrier(const XcdBarrier& b, const bool xb_leader) {
;     ...
;         const unsigned old = xb_add(&bar[XB_XSUB(b.x)], 1u);
;         const unsigned gen = old / nloc;
;         if (old + 1u == (gen + 1u) * nloc) {
;             __builtin_amdgcn_fence(__ATOMIC_RELEASE, "agent");
;             asm volatile("s_waitcnt vmcnt(0)" ::: "memory");
;             const unsigned og = xb_add(&bar[XB_TOP], 1u);
;             const unsigned tg = og / nx;
;             if (og + 1u == (tg + 1u) * nx) xb_add(&bar[XB_TOPGEN], 1u);
;             else XB_SPIN(xb_ld(&bar[XB_TOPGEN]) == tg, bar);
;             __builtin_amdgcn_fence(__ATOMIC_ACQUIRE, "agent");
;             xb_add(&bar[XB_XGEN(b.x)], 1u);
;             asm volatile("s_waitcnt vmcnt(0)" ::: "memory");
;         } else {
;             XB_SPIN(xb_ld(&bar[XB_XGEN(b.x)]) == gen, bar);
;             __builtin_amdgcn_fence(__ATOMIC_ACQUIRE, "agent");
.LBB0_180:
	s_or_b64 exec, exec, s[10:11]
	v_cvt_f32_u32_e32 v2, v9
	s_waitcnt vmcnt(0)
	v_readfirstlane_b32 s3, v1
	v_sub_u32_e32 v1, 0, v9
	v_rcp_iflag_f32_e32 v2, v2
	v_add_u32_e32 v3, s3, v0
	v_mul_f32_e32 v2, 0x4f7ffffe, v2
	v_cvt_u32_f32_e32 v2, v2
	v_mul_lo_u32 v0, v1, v2
	v_mul_hi_u32 v0, v2, v0
	v_add_u32_e32 v0, v2, v0
	v_mul_hi_u32 v0, v3, v0
	v_mul_lo_u32 v1, v0, v9
	v_sub_u32_e32 v1, v3, v1
	v_add_u32_e32 v2, 1, v0
	v_cmp_ge_u32_e32 vcc, v1, v9
	s_nop 1
	v_cndmask_b32_e32 v0, v0, v2, vcc
	v_sub_u32_e32 v2, v1, v9
	v_cndmask_b32_e32 v1, v1, v2, vcc
	v_add_u32_e32 v2, 1, v0
	v_cmp_ge_u32_e32 vcc, v1, v9
	v_add_u32_e32 v1, 1, v3
	s_nop 0
	v_cndmask_b32_e32 v0, v0, v2, vcc
	v_mul_lo_u32 v2, v9, v0
	v_add_u32_e32 v2, v2, v9
	v_cmp_ne_u32_e32 vcc, v1, v2
	s_and_saveexec_b64 s[8:9], vcc
	s_xor_b64 s[8:9], exec, s[8:9]
	s_cbranch_execz .LBB0_194
	v_mov_b32_e32 v1, 0x3100
	global_load_dword v1, v1, s[28:29] offset:1024 sc1
	s_add_u32 s12, s28, 0x3500
	s_addc_u32 s13, s29, 0
	s_waitcnt vmcnt(0)
	v_cmp_eq_u32_e32 vcc, v1, v0
	s_and_saveexec_b64 s[10:11], vcc
	s_cbranch_execz .LBB0_193
	s_mov_b32 s3, 1
	s_mov_b64 s[14:15], 0
	v_mov_b32_e32 v1, 0
	s_branch .LBB0_184

; __device__ __forceinline__ unsigned xb_ld(unsigned* p)              { return __hip_atomic_load(p, __ATOMIC_RELAXED, __HIP_MEMORY_SCOPE_AGENT); }
; __device__ __forceinline__ unsigned xb_add(unsigned* p, unsigned v) { return __hip_atomic_fetch_add(p, v, __ATOMIC_RELAXED, __HIP_MEMORY_SCOPE_AGENT); }
; #define XB_SPIN(cond, bar) do { unsigned _sp = 0; while (cond) { __builtin_amdgcn_s_sleep(1); \
;     if ((++_sp & 255u) == 0u) { if (xb_ld(&(bar)[XB_TMO])) break; if (_sp > XB_SPIN_CAP) { atomicAdd(&(bar)[XB_TMO], 1u); break; } } } } while (0)
; __device__ __forceinline__ void xcd_barrier(const XcdBarrier& b, const bool xb_leader) {
;     ...
;         const unsigned old = xb_add(&bar[XB_XSUB(b.x)], 1u);
;         const unsigned gen = old / nloc;
;         if (old + 1u == (gen + 1u) * nloc) {
;             __builtin_amdgcn_fence(__ATOMIC_RELEASE, "agent");
;             asm volatile("s_waitcnt vmcnt(0)" ::: "memory");
;             const unsigned og = xb_add(&bar[XB_TOP], 1u);
;             const unsigned tg = og / nx;
;             if (og + 1u == (tg + 1u) * nx) xb_add(&bar[XB_TOPGEN], 1u);
;             else XB_SPIN(xb_ld(&bar[XB_TOPGEN]) == tg, bar);
;             __builtin_amdgcn_fence(__ATOMIC_ACQUIRE, "agent");
;             xb_add(&bar[XB_XGEN(b.x)], 1u);
;             asm volatile("s_waitcnt vmcnt(0)" ::: "memory");
;         } else {
;             XB_SPIN(xb_ld(&bar[XB_XGEN(b.x)]) == gen, bar);
;             __builtin_amdgcn_fence(__ATOMIC_ACQUIRE, "agent");
.LBB0_821:
	s_or_b64 exec, exec, s[8:9]
	v_cvt_f32_u32_e32 v2, v9
	s_waitcnt vmcnt(0)
	v_readfirstlane_b32 s3, v1
	v_sub_u32_e32 v1, 0, v9
	v_rcp_iflag_f32_e32 v2, v2
	v_add_u32_e32 v3, s3, v0
	v_mul_f32_e32 v2, 0x4f7ffffe, v2
	v_cvt_u32_f32_e32 v2, v2
	v_mul_lo_u32 v0, v1, v2
	v_mul_hi_u32 v0, v2, v0
	v_add_u32_e32 v0, v2, v0
	v_mul_hi_u32 v0, v3, v0
	v_mul_lo_u32 v1, v0, v9
	v_sub_u32_e32 v1, v3, v1
	v_add_u32_e32 v2, 1, v0
	v_cmp_ge_u32_e32 vcc, v1, v9
	s_nop 1
	v_cndmask_b32_e32 v0, v0, v2, vcc
	v_sub_u32_e32 v2, v1, v9
	v_cndmask_b32_e32 v1, v1, v2, vcc
	v_add_u32_e32 v2, 1, v0
	v_cmp_ge_u32_e32 vcc, v1, v9
	v_add_u32_e32 v1, 1, v3
	s_nop 0
	v_cndmask_b32_e32 v0, v0, v2, vcc
	v_mul_lo_u32 v2, v9, v0
	v_add_u32_e32 v2, v2, v9
	v_cmp_ne_u32_e32 vcc, v1, v2
	s_and_saveexec_b64 s[6:7], vcc
	s_xor_b64 s[6:7], exec, s[6:7]
	s_cbranch_execz .LBB0_835
	v_mov_b32_e32 v1, 0x3100
	global_load_dword v1, v1, s[28:29] offset:1024 sc1
	s_add_u32 s10, s28, 0x3500
	s_addc_u32 s11, s29, 0
	s_waitcnt vmcnt(0)
	v_cmp_eq_u32_e32 vcc, v1, v0
	s_and_saveexec_b64 s[8:9], vcc
	s_cbranch_execz .LBB0_834
	s_mov_b32 s3, 1
	s_mov_b64 s[12:13], 0
	v_mov_b32_e32 v1, 0
	s_branch .LBB0_825

; __device__ __forceinline__ unsigned xb_ld(unsigned* p)              { return __hip_atomic_load(p, __ATOMIC_RELAXED, __HIP_MEMORY_SCOPE_AGENT); }
; __device__ __forceinline__ unsigned xb_add(unsigned* p, unsigned v) { return __hip_atomic_fetch_add(p, v, __ATOMIC_RELAXED, __HIP_MEMORY_SCOPE_AGENT); }
; #define XB_SPIN(cond, bar) do { unsigned _sp = 0; while (cond) { __builtin_amdgcn_s_sleep(1); \
;     if ((++_sp & 255u) == 0u) { if (xb_ld(&(bar)[XB_TMO])) break; if (_sp > XB_SPIN_CAP) { atomicAdd(&(bar)[XB_TMO], 1u); break; } } } } while (0)
; __device__ __forceinline__ void xcd_barrier(const XcdBarrier& b, const bool xb_leader) {
;     ...
;         const unsigned old = xb_add(&bar[XB_XSUB(b.x)], 1u);
;         const unsigned gen = old / nloc;
;         if (old + 1u == (gen + 1u) * nloc) {
;             __builtin_amdgcn_fence(__ATOMIC_RELEASE, "agent");
;             asm volatile("s_waitcnt vmcnt(0)" ::: "memory");
;             const unsigned og = xb_add(&bar[XB_TOP], 1u);
;             const unsigned tg = og / nx;
;             if (og + 1u == (tg + 1u) * nx) xb_add(&bar[XB_TOPGEN], 1u);
;             else XB_SPIN(xb_ld(&bar[XB_TOPGEN]) == tg, bar);
;             __builtin_amdgcn_fence(__ATOMIC_ACQUIRE, "agent");
;             xb_add(&bar[XB_XGEN(b.x)], 1u);
;             asm volatile("s_waitcnt vmcnt(0)" ::: "memory");
;         } else {
;             XB_SPIN(xb_ld(&bar[XB_XGEN(b.x)]) == gen, bar);
;             __builtin_amdgcn_fence(__ATOMIC_ACQUIRE, "agent");
.LBB0_1592:
	s_or_b64 exec, exec, s[10:11]
	v_cvt_f32_u32_e32 v2, v9
	s_waitcnt vmcnt(0)
	v_readfirstlane_b32 s3, v1
	v_sub_u32_e32 v1, 0, v9
	v_rcp_iflag_f32_e32 v2, v2
	v_add_u32_e32 v3, s3, v0
	v_mul_f32_e32 v2, 0x4f7ffffe, v2
	v_cvt_u32_f32_e32 v2, v2
	v_mul_lo_u32 v0, v1, v2
	v_mul_hi_u32 v0, v2, v0
	v_add_u32_e32 v0, v2, v0
	v_mul_hi_u32 v0, v3, v0
	v_mul_lo_u32 v1, v0, v9
	v_sub_u32_e32 v1, v3, v1
	v_add_u32_e32 v2, 1, v0
	v_cmp_ge_u32_e32 vcc, v1, v9
	s_nop 1
	v_cndmask_b32_e32 v0, v0, v2, vcc
	v_sub_u32_e32 v2, v1, v9
	v_cndmask_b32_e32 v1, v1, v2, vcc
	v_add_u32_e32 v2, 1, v0
	v_cmp_ge_u32_e32 vcc, v1, v9
	v_add_u32_e32 v1, 1, v3
	s_nop 0
	v_cndmask_b32_e32 v0, v0, v2, vcc
	v_mul_lo_u32 v2, v9, v0
	v_add_u32_e32 v2, v2, v9
	v_cmp_ne_u32_e32 vcc, v1, v2
	s_and_saveexec_b64 s[6:7], vcc
	s_xor_b64 s[6:7], exec, s[6:7]
	s_cbranch_execz .LBB0_1606
	v_mov_b32_e32 v1, 0x3100
	global_load_dword v1, v1, s[28:29] offset:1024 sc1
	s_add_u32 s12, s28, 0x3500
	s_addc_u32 s13, s29, 0
	s_waitcnt vmcnt(0)
	v_cmp_eq_u32_e32 vcc, v1, v0
	s_and_saveexec_b64 s[10:11], vcc
	s_cbranch_execz .LBB0_1605
	s_mov_b32 s3, 1
	s_mov_b64 s[14:15], 0
	v_mov_b32_e32 v1, 0
	s_branch .LBB0_1596

; __device__ __forceinline__ unsigned xb_ld(unsigned* p)              { return __hip_atomic_load(p, __ATOMIC_RELAXED, __HIP_MEMORY_SCOPE_AGENT); }
; __device__ __forceinline__ unsigned xb_add(unsigned* p, unsigned v) { return __hip_atomic_fetch_add(p, v, __ATOMIC_RELAXED, __HIP_MEMORY_SCOPE_AGENT); }
; #define XB_SPIN(cond, bar) do { unsigned _sp = 0; while (cond) { __builtin_amdgcn_s_sleep(1); \
;     if ((++_sp & 255u) == 0u) { if (xb_ld(&(bar)[XB_TMO])) break; if (_sp > XB_SPIN_CAP) { atomicAdd(&(bar)[XB_TMO], 1u); break; } } } } while (0)
; __device__ __forceinline__ void xcd_barrier(const XcdBarrier& b, const bool xb_leader) {
;     ...
;         const unsigned old = xb_add(&bar[XB_XSUB(b.x)], 1u);
;         const unsigned gen = old / nloc;
;         if (old + 1u == (gen + 1u) * nloc) {
;             __builtin_amdgcn_fence(__ATOMIC_RELEASE, "agent");
;             asm volatile("s_waitcnt vmcnt(0)" ::: "memory");
;             const unsigned og = xb_add(&bar[XB_TOP], 1u);
;             const unsigned tg = og / nx;
;             if (og + 1u == (tg + 1u) * nx) xb_add(&bar[XB_TOPGEN], 1u);
;             else XB_SPIN(xb_ld(&bar[XB_TOPGEN]) == tg, bar);
;             __builtin_amdgcn_fence(__ATOMIC_ACQUIRE, "agent");
;             xb_add(&bar[XB_XGEN(b.x)], 1u);
;             asm volatile("s_waitcnt vmcnt(0)" ::: "memory");
;         } else {
;             XB_SPIN(xb_ld(&bar[XB_XGEN(b.x)]) == gen, bar);
;             __builtin_amdgcn_fence(__ATOMIC_ACQUIRE, "agent");
.LBB0_1908:
	s_or_b64 exec, exec, s[8:9]
	v_cvt_f32_u32_e32 v2, v9
	s_waitcnt vmcnt(0)
	v_readfirstlane_b32 s2, v1
	v_sub_u32_e32 v1, 0, v9
	v_rcp_iflag_f32_e32 v2, v2
	v_add_u32_e32 v3, s2, v0
	v_mul_f32_e32 v2, 0x4f7ffffe, v2
	v_cvt_u32_f32_e32 v2, v2
	v_mul_lo_u32 v0, v1, v2
	v_mul_hi_u32 v0, v2, v0
	v_add_u32_e32 v0, v2, v0
	v_mul_hi_u32 v0, v3, v0
	v_mul_lo_u32 v1, v0, v9
	v_sub_u32_e32 v1, v3, v1
	v_add_u32_e32 v2, 1, v0
	v_cmp_ge_u32_e32 vcc, v1, v9
	s_nop 1
	v_cndmask_b32_e32 v0, v0, v2, vcc
	v_sub_u32_e32 v2, v1, v9
	v_cndmask_b32_e32 v1, v1, v2, vcc
	v_add_u32_e32 v2, 1, v0
	v_cmp_ge_u32_e32 vcc, v1, v9
	v_add_u32_e32 v1, 1, v3
	s_nop 0
	v_cndmask_b32_e32 v0, v0, v2, vcc
	v_mul_lo_u32 v2, v9, v0
	v_add_u32_e32 v2, v2, v9
	v_cmp_ne_u32_e32 vcc, v1, v2
	s_and_saveexec_b64 s[2:3], vcc
	s_xor_b64 s[2:3], exec, s[2:3]
	s_cbranch_execz .LBB0_1922
	v_mov_b32_e32 v1, 0x3100
	global_load_dword v1, v1, s[28:29] offset:1024 sc1
	s_add_u32 s12, s28, 0x3500
	s_addc_u32 s13, s29, 0
	s_waitcnt vmcnt(0)
	v_cmp_eq_u32_e32 vcc, v1, v0
	s_and_saveexec_b64 s[8:9], vcc
	s_cbranch_execz .LBB0_1921
	s_mov_b32 s26, 1
	s_mov_b64 s[14:15], 0
	v_mov_b32_e32 v1, 0
	s_branch .LBB0_1912
